# 832 layer-1 expert-weight tiles moved from the up-projection conversion slot to the in-projection slot (109 workgroups there)
# speedup vs baseline: 1.0186x; 1.0032x over previous
; #define LAS __attribute__((address_space(3)))
; DI void phase_p0(const Args& A, LAS unsigned char* lds, int it0, int it1, int gw, int ngw, int wave, int lane) {
;     ...
;     auto desc = [&](int item) { F8Tile d; const int r = item - I_IN - I_OUT; const int le = r / (3 * I_E), q = r % (3 * I_E), which = q / I_E, t = q % I_E;
;         if (which < 2) { const int kb = t / 44, nb = t % 44, n0 = nb * 64;
;             d.W = A.in[which == 0 ? I_EW1 : I_EW3] + (size_t)le * DM * FF; d.N = FF; d.k0 = kb * 128; d.n0 = n0; d.dst = w13 + (size_t)le * 5632 * DM; d.Kd = DM; d.drow0 = (size_t)((n0 >> 7) * 256 + which * 128 + (n0 & 127)); }
;         else { const int kb = t / 16, nb = t % 16;
;             d.W = A.in[I_EW2] + (size_t)le * FF * DM; d.N = DM; d.k0 = kb * 128; d.n0 = nb * 64; d.dst = w2t + (size_t)le * DM * FF; d.Kd = FF; d.drow0 = (size_t)nb * 64; }
;         return d; };
;     if (it < it1) {
;         f32x4 ra[4][4], rb[4][4]; LAS unsigned char* sc8 = (LAS unsigned char*)scr;
;         F8Tile d = desc(it);
; template <int l> DI void run_layer(const Args& A, LAS unsigned char* lds, const XcdBarrier& bar, int lo, int hi, int G, int bid, int tid, int lane, int wave, int gw, int ngw, int gtid, int nthr) {
;     ...
;         const bool conv = (l == 0) && (G >= 2 * P0_XC1) && (G % 8 == 0); const int Gg = conv ? G - P0_XC1 : G;
;         if (conv && bid >= Gg) { __syncthreads(); phase_p0(A, lds, P0_W, P0_SPLIT, (bid - Gg) * NWAVES + wave, P0_XC1 * NWAVES, wave, lane); __syncthreads(); }
.LBB0_135:
	v_readlane_b32 s4, v235, 9
	v_readlane_b32 s6, v235, 11
	s_cmp_lt_i32 s6, 3
	v_readlane_b32 s7, v235, 12
	s_cselect_b64 s[0:1], -1, 0
	s_cmp_gt_i32 s6, 2
	v_readlane_b32 s5, v235, 10
	s_cselect_b64 s[2:3], -1, 0
	s_cmp_lt_i32 s7, 3
	s_cselect_b64 s[4:5], -1, 0
	s_or_b64 s[2:3], s[2:3], s[4:5]
	s_and_b64 vcc, exec, s[2:3]
	s_cbranch_vccnz .LBB0_194
	s_cmpk_lt_i32 s50, 0xd0
	v_readlane_b32 s4, v235, 57
	s_cselect_b64 s[2:3], -1, 0
	s_cmp_lg_u32 s4, 0
	s_cselect_b64 s[4:5], -1, 0
	s_or_b64 s[2:3], s[2:3], s[4:5]
	s_add_i32 s6, s50, 0xffffff93
	s_and_b64 s[4:5], s[2:3], exec
	s_cselect_b32 s28, s50, s6
	s_cmp_lt_i32 s92, s28
	s_cselect_b64 s[4:5], -1, 0
	s_or_b64 s[4:5], s[2:3], s[4:5]
	s_mov_b64 s[2:3], -1
	s_and_b64 vcc, exec, s[4:5]
	s_cbranch_vccnz .LBB0_169
	s_sub_i32 s2, s92, s28
	s_lshl_b32 s2, s2, 3
	v_readlane_b32 s3, v235, 52
	s_add_i32 s2, s2, s3
	s_cmpk_gt_u32 s2, 0x453f
	s_barrier
	s_cbranch_scc1 .LBB0_168
	v_readlane_b32 s4, v235, 9
	v_readlane_b32 s5, v235, 10
	s_add_u32 s20, s4, 0x1600000
	s_addc_u32 s21, s5, 0
	s_add_u32 s22, s4, 0x17600000
	s_addc_u32 s23, s5, 0
	s_and_b32 s3, s2, 0xffff
	s_mul_i32 s3, s3, 0xf83f
	s_lshr_b32 s5, s3, 26
	s_mul_i32 s3, s5, 0x420
	v_readlane_b32 s7, v235, 12
	s_sub_i32 s2, s2, s3
	s_and_b32 s7, s2, 0xffff
	s_mul_i32 s3, s7, 0xba2f
	s_lshr_b32 s3, s3, 24
	s_mulk_i32 s3, 0x160
	s_sub_i32 s12, s2, s3
	s_cmpk_gt_u32 s7, 0x2bf
	v_readlane_b32 s6, v235, 11
	s_cbranch_scc0 .LBB0_141
	s_and_b32 s3, 0xffff, s5
	v_readlane_b32 s36, v235, 0
	s_and_b32 s2, 0xffff, s12
	s_mul_i32 s4, s3, 0xb00000
	v_readlane_b32 s38, v235, 2
	v_readlane_b32 s39, v235, 3
	s_add_u32 s8, s38, s4
	s_addc_u32 s9, s39, 0
	s_lshl_b32 s4, s2, 3
	s_lshl_b32 s2, s2, 6
	s_and_b32 s6, s4, 0xf80
	s_and_b32 s4, s2, 0x3c0
	s_mul_i32 s3, s3, 0x2c0000
	s_add_u32 s10, s22, s3
	v_readlane_b32 s37, v235, 1
	v_readlane_b32 s40, v235, 4
	v_readlane_b32 s41, v235, 5
	v_readlane_b32 s42, v235, 6
	v_readlane_b32 s43, v235, 7
	s_addc_u32 s11, s23, 0
	s_cbranch_execz .LBB0_142
	v_mov_b32_e32 v130, s4
	s_movk_i32 s24, 0xb00
	s_movk_i32 s18, 0x400
	s_branch .LBB0_143

; DI void phase_p0(const Args& A, LAS unsigned char* lds, int it0, int it1, int gw, int ngw, int wave, int lane) {
;     ...
;     auto desc = [&](int item) { F8Tile d; const int r = item - I_IN - I_OUT; const int le = r / (3 * I_E), q = r % (3 * I_E), which = q / I_E, t = q % I_E;
;         if (which < 2) { const int kb = t / 44, nb = t % 44, n0 = nb * 64;
;             d.W = A.in[which == 0 ? I_EW1 : I_EW3] + (size_t)le * DM * FF; d.N = FF; d.k0 = kb * 128; d.n0 = n0; d.dst = w13 + (size_t)le * 5632 * DM; d.Kd = DM; d.drow0 = (size_t)((n0 >> 7) * 256 + which * 128 + (n0 & 127)); }
;         else { const int kb = t / 16, nb = t % 16;
;             d.W = A.in[I_EW2] + (size_t)le * FF * DM; d.N = DM; d.k0 = kb * 128; d.n0 = nb * 64; d.dst = w2t + (size_t)le * DM * FF; d.Kd = FF; d.drow0 = (size_t)nb * 64; }
;     ...
;         for (; it < it1; it += ngw) {
;             const bool vn = it + ngw < it1; F8Tile dn = d; if (vn) dn = desc(it + ngw);
.LBB0_145:
	s_add_i32 s26, s2, 0x368
	s_cmpk_lt_i32 s26, 0x4c00
	s_cselect_b64 s[16:17], -1, 0
	s_cmpk_gt_i32 s26, 0x4bff
	s_cselect_b64 s[14:15], -1, 0
	s_and_b64 vcc, exec, s[14:15]
	s_mov_b32 s27, s6
	s_cbranch_vccnz .LBB0_152
	s_addk_i32 s2, 0xfca8
	s_mul_hi_i32 s3, s2, 0x3e0f83e1
	s_lshr_b32 s4, s3, 31
	s_ashr_i32 s7, s3, 8
	s_add_i32 s7, s7, s4
	s_mul_i32 s3, s7, 0x420
	s_sub_i32 s29, s2, s3
	s_mul_i32 s2, s29, 0xba3
	s_lshr_b32 s3, s2, 31
	s_ashr_i32 s34, s2, 20
	s_add_i32 s34, s34, s3
	s_mul_i32 s2, s34, 0x160
	s_sub_i32 s33, s29, s2
	s_mov_b64 s[18:19], -1
	s_cmpk_gt_i32 s29, 0x2bf
	s_sext_i32_i16 s35, s33
	s_mul_hi_i32 s30, s7, 0xb00000
	s_mul_i32 s31, s7, 0xb00000
	s_cbranch_scc0 .LBB0_148
	v_readlane_b32 s36, v235, 0
	v_readlane_b32 s38, v235, 2
	v_readlane_b32 s39, v235, 3
	s_add_u32 s8, s38, s31
	s_addc_u32 s9, s39, s30
	s_lshl_b32 s2, s35, 3
	s_and_b32 s27, s2, 0xf80
	s_lshl_b32 s2, s35, 6
	s_and_b32 s4, s2, 0x3c0
	s_mul_i32 s3, s7, 0x2c0000
	s_mul_hi_i32 s2, s7, 0x2c0000
	s_add_u32 s12, s22, s3
	v_readlane_b32 s37, v235, 1
	v_readlane_b32 s40, v235, 4
	v_readlane_b32 s41, v235, 5
	v_readlane_b32 s42, v235, 6
	v_readlane_b32 s43, v235, 7
	s_addc_u32 s13, s23, s2
	s_mov_b64 s[18:19], 0
	s_mov_b64 s[2:3], s[4:5]

; #define LAS __attribute__((address_space(3)))
; DI void phase_p0(const Args& A, LAS unsigned char* lds, int it0, int it1, int gw, int ngw, int wave, int lane) {
;     ...
;     if (it < it1) {
;         f32x4 ra[4][4], rb[4][4]; LAS unsigned char* sc8 = (LAS unsigned char*)scr;
;         F8Tile d = desc(it);
; template <int l> DI void run_layer(const Args& A, LAS unsigned char* lds, const XcdBarrier& bar, int lo, int hi, int G, int bid, int tid, int lane, int wave, int gw, int ngw, int gtid, int nthr) {
;     ...
;         const bool conv = (l == 0) && (P0_SPLIT < P0_END) && (G >= 2 * P0_XC) && (G % 8 == 0); const int Gg = conv ? G - P0_XC : G;
;         if (conv && bid >= Gg) { __syncthreads(); phase_p0(A, lds, P0_SPLIT, P0_END, (bid - Gg) * NWAVES + wave, P0_XC * NWAVES, wave, lane); __syncthreads(); }
.LBB0_1337:
	s_cmp_lt_i32 s6, 10
	s_cselect_b64 s[8:9], -1, 0
	s_and_b64 s[0:1], s[8:9], s[0:1]
	s_andn2_b64 vcc, exec, s[0:1]
	s_cbranch_vccnz .LBB0_1395
	s_cmpk_lt_i32 s50, 0xa0
	v_readlane_b32 s2, v235, 57
	s_cselect_b64 s[0:1], -1, 0
	s_cmp_lg_u32 s2, 0
	s_cselect_b64 s[2:3], -1, 0
	s_or_b64 s[0:1], s[0:1], s[2:3]
	s_add_i32 s4, s50, 0xffffffb0
	s_and_b64 s[2:3], s[0:1], exec
	s_cselect_b32 s30, s50, s4
	s_cmp_lt_i32 s92, s30
	s_cselect_b64 s[2:3], -1, 0
	s_or_b64 s[2:3], s[0:1], s[2:3]
	s_mov_b64 s[0:1], -1
	s_and_b64 vcc, exec, s[2:3]
	s_cbranch_vccnz .LBB0_1371
	s_sub_i32 s0, s92, s30
	s_lshl_b32 s0, s0, 3
	v_readlane_b32 s1, v235, 52
	s_add_i32 s0, s0, s1
	s_cmpk_gt_u32 s0, 0x3ebf
	s_waitcnt vmcnt(0)
	s_barrier
	s_cbranch_scc1 .LBB0_1370
	v_readlane_b32 s4, v235, 9
	v_readlane_b32 s5, v235, 10
	s_add_u32 s18, s4, 0x1600000
	s_addc_u32 s19, s5, 0
	s_add_u32 s20, s4, 0x17600000
	s_addc_u32 s21, s5, 0
	s_addk_i32 s0, 0x4540
	s_and_b32 s1, s0, 0xffff
	s_mul_i32 s1, s1, 0xf83f
	s_lshr_b32 s1, s1, 26
	s_mul_i32 s2, s1, 0x420
	s_sub_i32 s0, s0, s2
	s_and_b32 s5, s0, 0xffff
	s_mul_i32 s2, s5, 0xba2f
	s_lshr_b32 s2, s2, 24
	s_mulk_i32 s2, 0x160
	s_sub_i32 s12, s0, s2
	s_cmpk_gt_u32 s5, 0x2bf
	v_readlane_b32 s6, v235, 11
	v_readlane_b32 s7, v235, 12
	s_cbranch_scc0 .LBB0_1343
	s_and_b32 s2, 0xffff, s1
	v_readlane_b32 s36, v235, 0
	s_and_b32 s0, 0xffff, s12
	s_mul_i32 s3, s2, 0xb00000
	v_readlane_b32 s38, v235, 2
	v_readlane_b32 s39, v235, 3
	s_add_u32 s6, s38, s3
	s_addc_u32 s7, s39, 0
	s_lshl_b32 s3, s0, 3
	s_lshl_b32 s0, s0, 6
	s_and_b32 s4, s3, 0xf80
	s_and_b32 s0, s0, 0x3c0
	s_mul_i32 s2, s2, 0x2c0000
	s_add_u32 s10, s20, s2
	v_readlane_b32 s37, v235, 1
	v_readlane_b32 s40, v235, 4
	v_readlane_b32 s41, v235, 5
	v_readlane_b32 s42, v235, 6
	v_readlane_b32 s43, v235, 7
	s_addc_u32 s11, s21, 0
	s_cbranch_execz .LBB0_1344
	v_mov_b32_e32 v130, s0
	s_movk_i32 s22, 0xb00
	s_movk_i32 s16, 0x400
	s_branch .LBB0_1345

; DI void f8_load(f32x4 (&v)[4][4], const F8Tile& d, int hb, int lane) {
;     const int nq = lane & 15, kq = lane >> 4;
; #pragma unroll
;     for (int it = 0; it < 4; ++it)
; #pragma unroll
;         for (int j = 0; j < 4; ++j) v[it][j] = __builtin_nontemporal_load((const f32x4*)(d.W + (size_t)(d.k0 + hb * 64 + it * 16 + kq * 4 + j) * d.N + d.n0 + 4 * nq));
; }
.LBB0_1345:
	v_lshrrev_b32_e32 v2, 2, v146
	v_and_b32_e32 v1, 12, v2
	v_or_b32_e32 v187, 0x72, v1
	v_or_b32_e32 v188, 0x73, v2
	v_mov_b32_e32 v135, 0
	v_or_b32_e32 v159, 3, v2
	v_or_b32_e32 v163, 19, v2
	v_or_b32_e32 v167, 35, v2
	v_or_b32_e32 v172, 51, v2
	v_or_b32_e32 v176, 0x43, v2
	v_or_b32_e32 v180, 0x53, v2
	v_or_b32_e32 v184, 0x63, v2
	v_add_u32_e32 v2, s4, v188
	v_add_u32_e32 v4, s4, v187
	s_mov_b32 s1, 0
	v_lshlrev_b32_e32 v3, 2, v0
	v_mul_u32_u24_e32 v134, s16, v2
	v_mul_u32_u24_e32 v4, s16, v4
	v_mov_b32_e32 v5, v135
	v_and_b32_e32 v132, 60, v3
	v_lshl_add_u64 v[2:3], v[134:135], 2, s[6:7]
	s_lshl_b64 s[2:3], s[0:1], 2
	v_lshl_add_u64 v[4:5], v[4:5], 2, s[6:7]
	v_lshl_add_u64 v[2:3], v[2:3], 0, s[2:3]
	v_lshlrev_b32_e32 v134, 2, v132
	v_lshl_add_u64 v[4:5], v[4:5], 0, s[2:3]
	v_or_b32_e32 v183, 0x62, v1
	v_or_b32_e32 v185, 0x70, v1
	v_or_b32_e32 v186, 0x71, v1
	v_lshl_add_u64 v[2:3], v[2:3], 0, v[134:135]
	v_lshl_add_u64 v[4:5], v[4:5], 0, v[134:135]
	global_load_dwordx4 v[10:13], v[2:3], off nt
	global_load_dwordx4 v[14:17], v[4:5], off nt
	v_add_u32_e32 v2, s4, v186
	v_add_u32_e32 v4, s4, v185
	v_add_u32_e32 v18, s4, v184
	v_add_u32_e32 v20, s4, v183
	v_mul_u32_u24_e32 v2, s16, v2
	v_mov_b32_e32 v3, v135
	v_mul_u32_u24_e32 v4, s16, v4
	v_mov_b32_e32 v5, v135
	v_mul_u32_u24_e32 v18, s16, v18
	v_mov_b32_e32 v19, v135
	v_mul_u32_u24_e32 v20, s16, v20
	v_mov_b32_e32 v21, v135
	v_lshl_add_u64 v[2:3], v[2:3], 2, s[6:7]
	v_lshl_add_u64 v[4:5], v[4:5], 2, s[6:7]
	v_lshl_add_u64 v[18:19], v[18:19], 2, s[6:7]
	v_lshl_add_u64 v[20:21], v[20:21], 2, s[6:7]
	v_lshl_add_u64 v[2:3], v[2:3], 0, s[2:3]
	v_lshl_add_u64 v[4:5], v[4:5], 0, s[2:3]
	v_lshl_add_u64 v[18:19], v[18:19], 0, s[2:3]
	v_lshl_add_u64 v[20:21], v[20:21], 0, s[2:3]
	v_or_b32_e32 v179, 0x52, v1
	v_or_b32_e32 v181, 0x60, v1
	v_or_b32_e32 v182, 0x61, v1
	v_lshl_add_u64 v[2:3], v[2:3], 0, v[134:135]
	v_lshl_add_u64 v[6:7], v[4:5], 0, v[134:135]
	v_lshl_add_u64 v[18:19], v[18:19], 0, v[134:135]
	v_lshl_add_u64 v[20:21], v[20:21], 0, v[134:135]
	global_load_dwordx4 v[2:5], v[2:3], off nt
	s_nop 0
	global_load_dwordx4 v[6:9], v[6:7], off nt
	s_nop 0
	global_load_dwordx4 v[26:29], v[18:19], off nt
	global_load_dwordx4 v[30:33], v[20:21], off nt
	v_add_u32_e32 v18, s4, v182
	v_add_u32_e32 v20, s4, v181
	v_add_u32_e32 v34, s4, v180
	v_add_u32_e32 v36, s4, v179
	v_mul_u32_u24_e32 v18, s16, v18
	v_mov_b32_e32 v19, v135
	v_mul_u32_u24_e32 v20, s16, v20
	v_mov_b32_e32 v21, v135
	v_mul_u32_u24_e32 v34, s16, v34
	v_mov_b32_e32 v35, v135
	v_mul_u32_u24_e32 v36, s16, v36
	v_mov_b32_e32 v37, v135
	v_lshl_add_u64 v[18:19], v[18:19], 2, s[6:7]
	v_lshl_add_u64 v[20:21], v[20:21], 2, s[6:7]
	v_lshl_add_u64 v[34:35], v[34:35], 2, s[6:7]
	v_lshl_add_u64 v[36:37], v[36:37], 2, s[6:7]
	v_lshl_add_u64 v[18:19], v[18:19], 0, s[2:3]
	v_lshl_add_u64 v[20:21], v[20:21], 0, s[2:3]
	v_lshl_add_u64 v[34:35], v[34:35], 0, s[2:3]
	v_lshl_add_u64 v[36:37], v[36:37], 0, s[2:3]
	v_or_b32_e32 v175, 0x42, v1
	v_or_b32_e32 v177, 0x50, v1
	v_or_b32_e32 v178, 0x51, v1
	v_lshl_add_u64 v[18:19], v[18:19], 0, v[134:135]
	v_lshl_add_u64 v[22:23], v[20:21], 0, v[134:135]
	v_lshl_add_u64 v[34:35], v[34:35], 0, v[134:135]
	v_lshl_add_u64 v[36:37], v[36:37], 0, v[134:135]
	global_load_dwordx4 v[18:21], v[18:19], off nt
	s_nop 0
	global_load_dwordx4 v[22:25], v[22:23], off nt
	s_nop 0
	global_load_dwordx4 v[42:45], v[34:35], off nt
	global_load_dwordx4 v[46:49], v[36:37], off nt
	v_add_u32_e32 v34, s4, v178
	v_add_u32_e32 v36, s4, v177
	v_add_u32_e32 v50, s4, v176
	v_add_u32_e32 v52, s4, v175
	v_mul_u32_u24_e32 v34, s16, v34
	v_mov_b32_e32 v35, v135
	v_mul_u32_u24_e32 v36, s16, v36
	v_mov_b32_e32 v37, v135
	v_mul_u32_u24_e32 v50, s16, v50
	v_mov_b32_e32 v51, v135
	v_mul_u32_u24_e32 v52, s16, v52
	v_mov_b32_e32 v53, v135
	v_lshl_add_u64 v[34:35], v[34:35], 2, s[6:7]
	v_lshl_add_u64 v[36:37], v[36:37], 2, s[6:7]
	v_lshl_add_u64 v[50:51], v[50:51], 2, s[6:7]
	v_lshl_add_u64 v[52:53], v[52:53], 2, s[6:7]
	v_lshl_add_u64 v[34:35], v[34:35], 0, s[2:3]
	v_lshl_add_u64 v[36:37], v[36:37], 0, s[2:3]
	v_lshl_add_u64 v[50:51], v[50:51], 0, s[2:3]
	v_lshl_add_u64 v[52:53], v[52:53], 0, s[2:3]
	v_or_b32_e32 v171, 50, v1
	v_or_b32_e32 v173, 64, v1
	v_or_b32_e32 v174, 0x41, v1
	v_lshl_add_u64 v[34:35], v[34:35], 0, v[134:135]
	v_lshl_add_u64 v[38:39], v[36:37], 0, v[134:135]
	v_lshl_add_u64 v[50:51], v[50:51], 0, v[134:135]
	v_lshl_add_u64 v[52:53], v[52:53], 0, v[134:135]
	global_load_dwordx4 v[34:37], v[34:35], off nt
	s_nop 0
	global_load_dwordx4 v[38:41], v[38:39], off nt
	s_nop 0
	global_load_dwordx4 v[58:61], v[50:51], off nt
	global_load_dwordx4 v[62:65], v[52:53], off nt
	v_add_u32_e32 v50, s4, v174
	v_add_u32_e32 v52, s4, v173
	v_add_u32_e32 v66, s4, v172
	v_add_u32_e32 v68, s4, v171
	v_mul_u32_u24_e32 v50, s16, v50
	v_mov_b32_e32 v51, v135
	v_mul_u32_u24_e32 v52, s16, v52
	v_mov_b32_e32 v53, v135
	v_mul_u32_u24_e32 v66, s16, v66
	v_mov_b32_e32 v67, v135
	v_mul_u32_u24_e32 v68, s16, v68
	v_mov_b32_e32 v69, v135
	v_lshl_add_u64 v[50:51], v[50:51], 2, s[6:7]
	v_lshl_add_u64 v[52:53], v[52:53], 2, s[6:7]
	v_lshl_add_u64 v[66:67], v[66:67], 2, s[6:7]
	v_lshl_add_u64 v[68:69], v[68:69], 2, s[6:7]
	v_lshl_add_u64 v[50:51], v[50:51], 0, s[2:3]
	v_lshl_add_u64 v[52:53], v[52:53], 0, s[2:3]
	v_lshl_add_u64 v[66:67], v[66:67], 0, s[2:3]
	v_lshl_add_u64 v[68:69], v[68:69], 0, s[2:3]
	v_or_b32_e32 v166, 34, v1
	v_or_b32_e32 v168, 48, v1
	v_or_b32_e32 v169, 49, v1
	v_lshl_add_u64 v[50:51], v[50:51], 0, v[134:135]
	v_lshl_add_u64 v[54:55], v[52:53], 0, v[134:135]
	v_lshl_add_u64 v[66:67], v[66:67], 0, v[134:135]
; #define LAS __attribute__((address_space(3)))
; DI void f8_load(f32x4 (&v)[4][4], const F8Tile& d, int hb, int lane) {
;     const int nq = lane & 15, kq = lane >> 4;
; #pragma unroll
;     for (int it = 0; it < 4; ++it)
; #pragma unroll
;         for (int j = 0; j < 4; ++j) v[it][j] = __builtin_nontemporal_load((const f32x4*)(d.W + (size_t)(d.k0 + hb * 64 + it * 16 + kq * 4 + j) * d.N + d.n0 + 4 * nq));
; }
; DI void phase_p0(const Args& A, LAS unsigned char* lds, int it0, int it1, int gw, int ngw, int wave, int lane) {
;     ...
;     if (it < it1) {
;         f32x4 ra[4][4], rb[4][4]; LAS unsigned char* sc8 = (LAS unsigned char*)scr;
;         F8Tile d = desc(it);
;         f8_load(ra, d, 0, lane); f8_load(rb, d, 1, lane);
;         for (; it < it1; it += ngw) {
;             const bool vn = it + ngw < it1; F8Tile dn = d; if (vn) dn = desc(it + ngw);
;             f8_convert_reload(ra, 0, F8_WSC, sc8, vn, dn, lane);
	v_lshl_add_u64 v[68:69], v[68:69], 0, v[134:135]
	global_load_dwordx4 v[50:53], v[50:51], off nt
	s_nop 0
	global_load_dwordx4 v[54:57], v[54:55], off nt
	s_nop 0
	global_load_dwordx4 v[78:81], v[66:67], off nt
	global_load_dwordx4 v[74:77], v[68:69], off nt
	v_add_u32_e32 v66, s4, v169
	v_add_u32_e32 v68, s4, v168
	v_add_u32_e32 v82, s4, v167
	v_add_u32_e32 v84, s4, v166
	v_mul_u32_u24_e32 v66, s16, v66
	v_mov_b32_e32 v67, v135
	v_mul_u32_u24_e32 v68, s16, v68
	v_mov_b32_e32 v69, v135
	v_mul_u32_u24_e32 v82, s16, v82
	v_mov_b32_e32 v83, v135
	v_mul_u32_u24_e32 v84, s16, v84
	v_mov_b32_e32 v85, v135
	v_lshl_add_u64 v[66:67], v[66:67], 2, s[6:7]
	v_lshl_add_u64 v[68:69], v[68:69], 2, s[6:7]
	v_lshl_add_u64 v[82:83], v[82:83], 2, s[6:7]
	v_lshl_add_u64 v[84:85], v[84:85], 2, s[6:7]
	v_lshl_add_u64 v[66:67], v[66:67], 0, s[2:3]
	v_lshl_add_u64 v[68:69], v[68:69], 0, s[2:3]
	v_lshl_add_u64 v[82:83], v[82:83], 0, s[2:3]
	v_lshl_add_u64 v[84:85], v[84:85], 0, s[2:3]
	v_or_b32_e32 v162, 18, v1
	v_or_b32_e32 v164, 32, v1
	v_or_b32_e32 v165, 33, v1
	v_lshl_add_u64 v[66:67], v[66:67], 0, v[134:135]
	v_lshl_add_u64 v[70:71], v[68:69], 0, v[134:135]
	v_lshl_add_u64 v[82:83], v[82:83], 0, v[134:135]
	v_lshl_add_u64 v[84:85], v[84:85], 0, v[134:135]
	global_load_dwordx4 v[66:69], v[66:67], off nt
	s_nop 0
	global_load_dwordx4 v[70:73], v[70:71], off nt
	s_nop 0
	global_load_dwordx4 v[90:93], v[82:83], off nt
	global_load_dwordx4 v[94:97], v[84:85], off nt
	v_add_u32_e32 v82, s4, v165
	v_add_u32_e32 v84, s4, v164
	v_add_u32_e32 v98, s4, v163
	v_add_u32_e32 v100, s4, v162
	v_mul_u32_u24_e32 v82, s16, v82
	v_mov_b32_e32 v83, v135
	v_mul_u32_u24_e32 v84, s16, v84
	v_mov_b32_e32 v85, v135
	v_mul_u32_u24_e32 v98, s16, v98
	v_mov_b32_e32 v99, v135
	v_mul_u32_u24_e32 v100, s16, v100
	v_mov_b32_e32 v101, v135
	v_lshl_add_u64 v[82:83], v[82:83], 2, s[6:7]
	v_lshl_add_u64 v[84:85], v[84:85], 2, s[6:7]
	v_lshl_add_u64 v[98:99], v[98:99], 2, s[6:7]
	v_lshl_add_u64 v[100:101], v[100:101], 2, s[6:7]
	v_lshl_add_u64 v[82:83], v[82:83], 0, s[2:3]
	v_lshl_add_u64 v[84:85], v[84:85], 0, s[2:3]
	v_lshl_add_u64 v[98:99], v[98:99], 0, s[2:3]
	v_lshl_add_u64 v[100:101], v[100:101], 0, s[2:3]
	v_or_b32_e32 v158, 2, v1
	v_or_b32_e32 v160, 16, v1
	v_or_b32_e32 v161, 17, v1
	v_lshl_add_u64 v[82:83], v[82:83], 0, v[134:135]
	v_lshl_add_u64 v[86:87], v[84:85], 0, v[134:135]
	v_lshl_add_u64 v[98:99], v[98:99], 0, v[134:135]
	v_lshl_add_u64 v[100:101], v[100:101], 0, v[134:135]
	global_load_dwordx4 v[82:85], v[82:83], off nt
	s_nop 0
	global_load_dwordx4 v[86:89], v[86:87], off nt
	s_nop 0
	global_load_dwordx4 v[106:109], v[98:99], off nt
	global_load_dwordx4 v[110:113], v[100:101], off nt
	v_add_u32_e32 v98, s4, v161
	v_add_u32_e32 v100, s4, v160
	v_add_u32_e32 v114, s4, v159
	v_add_u32_e32 v116, s4, v158
	v_mul_u32_u24_e32 v98, s16, v98
	v_mov_b32_e32 v99, v135
	v_mul_u32_u24_e32 v100, s16, v100
	v_mov_b32_e32 v101, v135
	v_mul_u32_u24_e32 v114, s16, v114
	v_mov_b32_e32 v115, v135
	v_mul_u32_u24_e32 v116, s16, v116
	v_mov_b32_e32 v117, v135
	v_lshl_add_u64 v[98:99], v[98:99], 2, s[6:7]
	v_lshl_add_u64 v[100:101], v[100:101], 2, s[6:7]
	v_lshl_add_u64 v[114:115], v[114:115], 2, s[6:7]
	v_lshl_add_u64 v[116:117], v[116:117], 2, s[6:7]
	v_lshl_add_u64 v[98:99], v[98:99], 0, s[2:3]
	v_lshl_add_u64 v[100:101], v[100:101], 0, s[2:3]
	v_lshl_add_u64 v[114:115], v[114:115], 0, s[2:3]
	v_lshl_add_u64 v[116:117], v[116:117], 0, s[2:3]
	v_or_b32_e32 v133, 1, v1
	v_lshl_add_u64 v[98:99], v[98:99], 0, v[134:135]
	v_lshl_add_u64 v[102:103], v[100:101], 0, v[134:135]
	v_lshl_add_u64 v[114:115], v[114:115], 0, v[134:135]
	v_lshl_add_u64 v[116:117], v[116:117], 0, v[134:135]
	global_load_dwordx4 v[98:101], v[98:99], off nt
	s_nop 0
	global_load_dwordx4 v[102:105], v[102:103], off nt
	s_nop 0
	global_load_dwordx4 v[122:125], v[114:115], off nt
	global_load_dwordx4 v[126:129], v[116:117], off nt
	v_add_u32_e32 v114, s4, v133
	v_add_u32_e32 v116, s4, v1
	v_mul_u32_u24_e32 v114, s16, v114
	v_mov_b32_e32 v115, v135
	v_mul_u32_u24_e32 v116, s16, v116
	v_mov_b32_e32 v117, v135
	v_lshl_add_u64 v[114:115], v[114:115], 2, s[6:7]
	v_lshl_add_u64 v[116:117], v[116:117], 2, s[6:7]
	v_lshl_add_u64 v[114:115], v[114:115], 0, s[2:3]
	v_lshl_add_u64 v[116:117], v[116:117], 0, s[2:3]
	v_lshl_add_u64 v[114:115], v[114:115], 0, v[134:135]
	v_lshl_add_u64 v[118:119], v[116:117], 0, v[134:135]
	global_load_dwordx4 v[114:117], v[114:115], off nt
	s_nop 0
	global_load_dwordx4 v[118:121], v[118:119], off nt
	v_readlane_b32 s2, v235, 52
	s_mulk_i32 s2, 0x4200
	v_lshlrev_b32_e32 v137, 4, v0
	s_add_i32 s2, s2, 0
	v_and_b32_e32 v138, 0x70, v137
	v_add_u32_e32 v134, s2, v1
	v_lshrrev_b32_e32 v136, 3, v146
	v_add_u32_e32 v157, s2, v138
	s_lshl_b32 s2, s30, 3
	v_readlane_b32 s12, v235, 54
	v_mov_b32_e32 v131, v135
	v_mul_u32_u24_e32 v156, 0x84, v132
	v_mul_u32_u24_e32 v189, 0x84, v136
	v_readlane_b32 s13, v235, 55
	s_sub_i32 s2, s12, s2
	v_mov_b32_e32 v139, v135
	v_mov_b32_e32 v137, v135
	v_or_b32_e32 v140, 8, v136
	v_mov_b32_e32 v141, v135
	v_or_b32_e32 v142, 16, v136
	v_mov_b32_e32 v143, v135
	v_or_b32_e32 v144, 24, v136
	v_mov_b32_e32 v145, v135
	v_or_b32_e32 v148, 32, v136
	v_mov_b32_e32 v149, v135
	v_or_b32_e32 v150, 40, v136
	v_mov_b32_e32 v151, v135
	v_or_b32_e32 v152, 48, v136
	v_mov_b32_e32 v153, v135
	v_or_b32_e32 v154, 56, v136
	v_mov_b32_e32 v155, v135
	s_add_i32 s23, s2, 0x47c0
	s_mov_b32 s24, 0xc3e00000
	v_add_u32_e32 v189, v157, v189
	v_mov_b32_e32 v190, 0x43e00000
	v_add_u32_e32 v191, v134, v156
	v_mov_b64_e32 v[156:157], v[130:131]
	s_mov_b32 s17, s22
	s_mov_b64 s[12:13], s[10:11]
	s_waitcnt vmcnt(0)
	s_branch .LBB0_1347
